# attention near path: 16 ds_read2_b32 instead of 32 ds_read_b32, waits recounted per consumer
# speedup vs baseline: 1.0091x; 1.0057x over previous
;     ...
;                 float mx = -1e30f;
;                 if (__any(qrel <= 64 * ck + 191)) {
; #pragma unroll
;                     for (int k2 = 0; k2 < 2; ++k2) {
;                         float bb[16];
; #pragma unroll
;                         for (int i = 0; i < 16; ++i) { const int key = 32 * (2 * ck + k2) + (i & 3) + 8 * (i >> 2) + 4 * half; const int n = qrel - key;
;                             bb[i] = LUT[1 + (n < -1 ? -1 : (n > 128 ? 128 : n))]; }
; #pragma unroll
;                         for (int i = 0; i < 16; ++i) asm volatile("" : "+v"(bb[i]));
; #pragma unroll
;                         for (int i = 0; i < 16; ++i) { const float s = sacc[k2][i] + bb[i]; sacc[k2][i] = s; mx = fmaxf(mx, s); } }
;                 } else {
; #pragma unroll
;                     for (int k2 = 0; k2 < 2; ++k2)
; #pragma unroll
;                         for (int i = 0; i < 16; ++i) { const float s = sacc[k2][i] + bfar; sacc[k2][i] = s; mx = fmaxf(mx, s); }
;                 }
.LBB0_2230:
	v_mov_b32_e32 v64, v250
	s_waitcnt lgkmcnt(0)
	ds_read_b128 v[32:35], v251
	ds_read_b128 v[66:69], v251 offset:32
	ds_read_b128 v[70:73], v251 offset:64
	ds_read_b128 v[74:77], v251 offset:96
	ds_read_b128 v[78:81], v251 offset:4608
	ds_read_b128 v[122:125], v251 offset:4640
	v_cmp_ge_i32_e32 vcc, s22, v64
	s_waitcnt lgkmcnt(5)
	v_mfma_f32_32x32x16_bf16 v[48:63], v[32:35], v[110:113], 0
	s_waitcnt lgkmcnt(4)
	v_mfma_f32_32x32x16_bf16 v[48:63], v[66:69], v[106:109], v[48:63]
	ds_read_b128 v[66:69], v251 offset:4672
	s_waitcnt lgkmcnt(4)
	v_mfma_f32_32x32x16_bf16 v[48:63], v[70:73], v[102:105], v[48:63]
	ds_read_b128 v[70:73], v251 offset:4704
	s_waitcnt lgkmcnt(4)
	v_mfma_f32_32x32x16_bf16 v[48:63], v[74:77], v[98:101], v[48:63]
	s_waitcnt lgkmcnt(3)
	v_mfma_f32_32x32x16_bf16 v[32:47], v[78:81], v[110:113], 0
	s_waitcnt lgkmcnt(2)
	v_mfma_f32_32x32x16_bf16 v[32:47], v[122:125], v[106:109], v[32:47]
	s_waitcnt lgkmcnt(1)
	v_mfma_f32_32x32x16_bf16 v[32:47], v[66:69], v[102:105], v[32:47]
	s_waitcnt lgkmcnt(0)
	v_mfma_f32_32x32x16_bf16 v[32:47], v[70:73], v[98:101], v[32:47]
	s_cbranch_vccz .LBB0_2237
	v_add3_u32 v64, v155, v64, s21
	v_med3_i32 v235, v64, -1, s98
	v_lshl_add_u32 v235, v235, 2, s99
	ds_read2_b32 v[122:123], v235 offset0:59 offset1:58
	ds_read2_b32 v[124:125], v235 offset0:57 offset1:56
	ds_read2_b32 v[126:127], v235 offset0:51 offset1:50
	ds_read2_b32 v[128:129], v235 offset0:49 offset1:48
	ds_read2_b32 v[130:131], v235 offset0:43 offset1:42
	ds_read2_b32 v[132:133], v235 offset0:41 offset1:40
	ds_read2_b32 v[134:135], v235 offset0:35 offset1:34
	ds_read2_b32 v[136:137], v235 offset0:33 offset1:32
	s_waitcnt lgkmcnt(7)
	v_add_f32_e32 v122, v48, v122
	v_add_f32_e32 v123, v49, v123
	v_max3_f32 v138, v122, s23, v123
	s_waitcnt lgkmcnt(6)
	v_add_f32_e32 v124, v50, v124
	v_add_f32_e32 v125, v51, v125
	v_max3_f32 v138, v138, v124, v125
	s_waitcnt lgkmcnt(5)
	v_add_f32_e32 v126, v52, v126
	v_add_f32_e32 v127, v53, v127
	v_max3_f32 v138, v138, v126, v127
	s_waitcnt lgkmcnt(4)
	v_add_f32_e32 v128, v54, v128
	v_add_f32_e32 v129, v55, v129
	v_max3_f32 v138, v138, v128, v129
	s_waitcnt lgkmcnt(3)
	v_add_f32_e32 v130, v56, v130
	v_add_f32_e32 v131, v57, v131
	v_max3_f32 v138, v138, v130, v131
	s_waitcnt lgkmcnt(2)
	v_add_f32_e32 v132, v58, v132
	v_add_f32_e32 v133, v59, v133
	v_max3_f32 v138, v138, v132, v133
	s_waitcnt lgkmcnt(1)
	v_add_f32_e32 v134, v60, v134
	v_add_f32_e32 v135, v61, v135
	v_max3_f32 v138, v138, v134, v135
	s_waitcnt lgkmcnt(0)
	v_add_f32_e32 v136, v62, v136
	v_add_f32_e32 v137, v63, v137
	v_max3_f32 v166, v138, v136, v137
	ds_read2_b32 v[138:139], v235 offset0:27 offset1:26
	ds_read2_b32 v[140:141], v235 offset0:25 offset1:24
	ds_read2_b32 v[168:169], v235 offset0:19 offset1:18
	ds_read2_b32 v[170:171], v235 offset0:17 offset1:16
	ds_read2_b32 v[172:173], v235 offset0:11 offset1:10
	ds_read2_b32 v[174:175], v235 offset0:9 offset1:8
	ds_read2_b32 v[204:205], v235 offset0:3 offset1:2
	ds_read2_b32 v[226:227], v235 offset0:1 offset1:0
	s_waitcnt lgkmcnt(7)
	v_add_f32_e32 v164, v32, v138
	v_add_f32_e32 v165, v33, v139
	s_waitcnt lgkmcnt(5)
	v_add_f32_e32 v168, v36, v168
	v_add_f32_e32 v169, v37, v169
	v_max3_f32 v64, v166, v164, v165
	v_add_f32_e32 v166, v34, v140
	v_add_f32_e32 v167, v35, v141
	s_waitcnt lgkmcnt(4)
	v_add_f32_e32 v170, v38, v170
	v_add_f32_e32 v171, v39, v171
	v_max3_f32 v64, v64, v166, v167
	v_max3_f32 v64, v64, v168, v169
	v_max3_f32 v64, v64, v170, v171
	s_waitcnt lgkmcnt(3)
	v_add_f32_e32 v172, v40, v172
	v_add_f32_e32 v173, v41, v173
	s_waitcnt lgkmcnt(2)
	v_add_f32_e32 v174, v42, v174
	v_add_f32_e32 v175, v43, v175
	v_max3_f32 v64, v64, v172, v173
	v_max3_f32 v64, v64, v174, v175
	s_waitcnt lgkmcnt(1)
	v_add_f32_e32 v138, v44, v204
	v_add_f32_e32 v139, v45, v205
	v_max3_f32 v64, v64, v138, v139
	s_waitcnt lgkmcnt(0)
	v_add_f32_e32 v140, v46, v226
	v_add_f32_e32 v141, v47, v227
	v_max3_f32 v64, v64, v140, v141
	s_cbranch_execnz .LBB0_2233
